# v8 + P11: each wave owns 64 contiguous output columns (B fragment remap); epilogue stores 16 rows x 64 contiguous bytes per dwordx4
# baseline (speedup 1.0000x reference)
.LBB0_1348:
	s_add_u32 s10, s82, 0xc6800000
	s_addc_u32 s11, s83, 0
	s_lshl_b32 s12, s12, 5
	s_and_b32 s16, s12, 0x60
	s_mov_b64 s[12:13], 0x80
	s_add_i32 m0, s37, 0x18000
	v_lshl_add_u64 v[8:9], v[8:9], 0, s[12:13]
	s_lshl_b32 s15, s14, 13
	s_lshl_b32 s18, s16, 7
	s_waitcnt vmcnt(2)
	s_barrier
	global_load_lds_dwordx4 v[8:9], off
	v_lshl_add_u64 v[4:5], v[4:5], 0, s[12:13]
	s_add_i32 m0, s37, 0x1a000
	s_add_i32 s65, s37, 0x8000
	s_add_i32 s66, s37, 0xa000
	global_load_lds_dwordx4 v[4:5], off
	v_lshl_add_u64 v[2:3], v[2:3], 0, s[12:13]
	s_mov_b32 m0, s65
	s_add_u32 s20, s42, 0x40080
	global_load_lds_dwordx4 v[2:3], off
	v_lshl_add_u64 v[2:3], v[6:7], 0, s[12:13]
	s_mov_b32 m0, s66
	s_addc_u32 s21, s43, 0
	global_load_lds_dwordx4 v[2:3], off
	s_add_i32 m0, s37, 0x1c000
	v_lshl_add_u64 v[2:3], s[20:21], 0, v[200:201]
	global_load_lds_dwordx4 v[2:3], off
	v_lshl_add_u64 v[2:3], s[20:21], 0, v[194:195]
	s_add_i32 m0, s37, 0x1e000
	v_lshlrev_b32_e32 v4, 2, v0
	global_load_lds_dwordx4 v[2:3], off
	v_and_b32_e32 v2, 15, v0
	v_lshl_or_b32 v1, s14, 6, v2
	v_lshlrev_b32_e32 v3, 1, v13
	v_lshlrev_b32_e32 v5, 6, v0
	s_movk_i32 s14, 0x3c0
	v_lshl_or_b32 v2, v2, 6, v3
	v_and_b32_e32 v4, 32, v4
	v_and_or_b32 v3, v5, s14, v3
	v_bitop3_b32 v199, s18, v3, v4 bitop3:0xf6
	v_add_u32_e32 v199, s18, v199
	v_lshlrev_b32_e32 v3, 8, v0
	v_bitop3_b32 v2, v2, s15, v4 bitop3:0xde
	v_and_b32_e32 v3, 0x18000, v3
	v_lshlrev_b32_e32 v4, 11, v14
	v_or3_b32 v3, v11, v3, v4
	v_add_u32_e32 v204, v3, v12
	v_lshlrev_b32_e32 v3, 4, v10
	v_and_b32_e32 v3, 0x38000, v3
	s_mov_b64 s[20:21], 0x40080
	s_waitcnt vmcnt(6)
	s_cmpk_lt_u32 s9, 0x100
	v_or3_b32 v3, v11, v3, v4
	s_cselect_b64 s[14:15], -1, 0
	s_ashr_i32 s9, s8, 31
	v_lshl_add_u64 v[206:207], v[204:205], 0, s[20:21]
	v_add_u32_e32 v204, v3, v12
	v_add_u32_e32 v3, 0, v199
	s_mov_b32 s44, 0
	s_ashr_i32 s67, s80, 31
	v_lshl_or_b32 v224, s16, 1, v13
	v_lshl_add_u64 v[208:209], v[204:205], 0, s[20:21]
	v_mov_b64_e32 v[210:211], s[8:9]
	v_add_u32_e32 v225, 0x10000, v3
	v_add_u32_e32 v226, 0x11000, v3
	v_add_u32_e32 v227, 0, v2
	v_mov_b32_e32 v228, 0x7f7f7f7f
	s_mov_b32 s16, 0x3c800000
	s_mov_b32 s18, 0x41800000
	s_mov_b32 s68, 0x40000
	s_mov_b64 s[20:21], 0x48000
	s_mov_b32 s69, 0x48000
	s_mov_b64 s[22:23], 0x50000
	s_mov_b32 s70, 0x50000
	s_mov_b64 s[24:25], 0x58000
	s_mov_b32 s71, 0x58000
	s_barrier
	s_branch .LBB0_1351

.LBB0_1354:
	s_waitcnt lgkmcnt(0)
	s_barrier
	s_setprio 1
	s_waitcnt lgkmcnt(0)
	v_mfma_scale_f32_16x16x128_f8f6f4 v[126:129], v[26:33], v[58:65], v[126:129], v228, v228 op_sel_hi:[0,0,0]
	v_mfma_scale_f32_16x16x128_f8f6f4 v[122:125], v[18:25], v[58:65], v[122:125], v228, v228 op_sel_hi:[0,0,0]
	v_mfma_scale_f32_16x16x128_f8f6f4 v[114:117], v[26:33], v[50:57], v[114:117], v228, v228 op_sel_hi:[0,0,0]
	v_mfma_scale_f32_16x16x128_f8f6f4 v[106:109], v[18:25], v[50:57], v[106:109], v228, v228 op_sel_hi:[0,0,0]
	v_mfma_scale_f32_16x16x128_f8f6f4 v[98:101], v[26:33], v[42:49], v[98:101], v228, v228 op_sel_hi:[0,0,0]
	v_mfma_scale_f32_16x16x128_f8f6f4 v[90:93], v[18:25], v[42:49], v[90:93], v228, v228 op_sel_hi:[0,0,0]
	v_mfma_scale_f32_16x16x128_f8f6f4 v[82:85], v[26:33], v[34:41], v[82:85], v228, v228 op_sel_hi:[0,0,0]
	v_mfma_scale_f32_16x16x128_f8f6f4 v[74:77], v[18:25], v[34:41], v[74:77], v228, v228 op_sel_hi:[0,0,0]
	s_setprio 0
	s_setprio 1
	v_mfma_scale_f32_16x16x128_f8f6f4 v[118:121], v[10:17], v[58:65], v[118:121], v228, v228 op_sel_hi:[0,0,0]
	v_mfma_scale_f32_16x16x128_f8f6f4 v[110:113], v[2:9], v[58:65], v[110:113], v228, v228 op_sel_hi:[0,0,0]
	v_mfma_scale_f32_16x16x128_f8f6f4 v[102:105], v[10:17], v[50:57], v[102:105], v228, v228 op_sel_hi:[0,0,0]
	v_mfma_scale_f32_16x16x128_f8f6f4 v[94:97], v[2:9], v[50:57], v[94:97], v228, v228 op_sel_hi:[0,0,0]
	v_mfma_scale_f32_16x16x128_f8f6f4 v[86:89], v[10:17], v[42:49], v[86:89], v228, v228 op_sel_hi:[0,0,0]
	v_mfma_scale_f32_16x16x128_f8f6f4 v[78:81], v[2:9], v[42:49], v[78:81], v228, v228 op_sel_hi:[0,0,0]
	v_mfma_scale_f32_16x16x128_f8f6f4 v[70:73], v[10:17], v[34:41], v[70:73], v228, v228 op_sel_hi:[0,0,0]
	v_mfma_scale_f32_16x16x128_f8f6f4 v[66:69], v[2:9], v[34:41], v[66:69], v228, v228 op_sel_hi:[0,0,0]
	s_setprio 0
	s_barrier
	s_add_i32 s50, 0, 0x18000
	s_add_i32 s51, 0, 0x1c000
	v_add_u32_e32 v14, s50, v199
	v_add_u32_e32 v30, 0x1000, v14
	ds_read_b128 v[2:5], v14
	ds_read_b128 v[6:9], v14 offset:1024
	ds_read_b128 v[10:13], v14 offset:2048
	ds_read_b128 v[14:17], v14 offset:3072
	ds_read_b128 v[18:21], v30
	ds_read_b128 v[22:25], v30 offset:1024
	ds_read_b128 v[26:29], v30 offset:2048
	ds_read_b128 v[30:33], v30 offset:3072
	s_add_u32 s48, s48, 0x40000
	s_addc_u32 s49, s49, 0
	s_mov_b32 m0, s63
	v_lshl_add_u64 v[230:231], s[48:49], 0, v[202:203]
	ds_read_b128 v[34:37], v227 offset:32768
	ds_read_b128 v[38:41], v227 offset:33792
	ds_read_b128 v[42:45], v227 offset:34816
	ds_read_b128 v[46:49], v227 offset:35840
	ds_read_b128 v[50:53], v227 offset:36864
	ds_read_b128 v[54:57], v227 offset:37888
	ds_read_b128 v[58:61], v227 offset:38912
	ds_read_b128 v[62:65], v227 offset:39936
	global_load_lds_dwordx4 v[230:231], off
	v_lshl_add_u64 v[230:231], s[48:49], 0, v[196:197]
	s_mov_b32 m0, s64
	s_nop 0
	global_load_lds_dwordx4 v[230:231], off
	s_waitcnt vmcnt(8)
	s_waitcnt lgkmcnt(0)
	s_barrier
	s_setprio 1
	s_waitcnt lgkmcnt(0)
	v_mfma_scale_f32_16x16x128_f8f6f4 v[190:193], v[2:9], v[34:41], v[190:193], v228, v228 op_sel_hi:[0,0,0]
	v_mfma_scale_f32_16x16x128_f8f6f4 v[186:189], v[10:17], v[34:41], v[186:189], v228, v228 op_sel_hi:[0,0,0]
	v_mfma_scale_f32_16x16x128_f8f6f4 v[182:185], v[2:9], v[42:49], v[182:185], v228, v228 op_sel_hi:[0,0,0]
	v_mfma_scale_f32_16x16x128_f8f6f4 v[178:181], v[10:17], v[42:49], v[178:181], v228, v228 op_sel_hi:[0,0,0]
	v_mfma_scale_f32_16x16x128_f8f6f4 v[174:177], v[2:9], v[50:57], v[174:177], v228, v228 op_sel_hi:[0,0,0]
	v_mfma_scale_f32_16x16x128_f8f6f4 v[154:157], v[10:17], v[50:57], v[154:157], v228, v228 op_sel_hi:[0,0,0]
	v_mfma_scale_f32_16x16x128_f8f6f4 v[146:149], v[2:9], v[58:65], v[146:149], v228, v228 op_sel_hi:[0,0,0]
	v_mfma_scale_f32_16x16x128_f8f6f4 v[138:141], v[10:17], v[58:65], v[138:141], v228, v228 op_sel_hi:[0,0,0]
	s_setprio 0
	s_setprio 1
	v_mfma_scale_f32_16x16x128_f8f6f4 v[170:173], v[18:25], v[34:41], v[170:173], v228, v228 op_sel_hi:[0,0,0]
	v_mfma_scale_f32_16x16x128_f8f6f4 v[166:169], v[26:33], v[34:41], v[166:169], v228, v228 op_sel_hi:[0,0,0]
	v_mfma_scale_f32_16x16x128_f8f6f4 v[162:165], v[18:25], v[42:49], v[162:165], v228, v228 op_sel_hi:[0,0,0]
	v_mfma_scale_f32_16x16x128_f8f6f4 v[158:161], v[26:33], v[42:49], v[158:161], v228, v228 op_sel_hi:[0,0,0]
	v_mfma_scale_f32_16x16x128_f8f6f4 v[150:153], v[18:25], v[50:57], v[150:153], v228, v228 op_sel_hi:[0,0,0]
	v_mfma_scale_f32_16x16x128_f8f6f4 v[142:145], v[26:33], v[50:57], v[142:145], v228, v228 op_sel_hi:[0,0,0]
	v_mfma_scale_f32_16x16x128_f8f6f4 v[134:137], v[18:25], v[58:65], v[134:137], v228, v228 op_sel_hi:[0,0,0]
	v_mfma_scale_f32_16x16x128_f8f6f4 v[130:133], v[26:33], v[58:65], v[130:133], v228, v228 op_sel_hi:[0,0,0]
	s_setprio 0
	s_barrier
	s_add_i32 s48, s50, s56
	v_lshl_add_u64 v[222:223], v[222:223], 0, s[12:13]
	s_mov_b32 m0, s48
	ds_read_b128 v[34:37], v227 offset:49152
	ds_read_b128 v[38:41], v227 offset:50176
	ds_read_b128 v[42:45], v227 offset:51200
	ds_read_b128 v[46:49], v227 offset:52224
	ds_read_b128 v[50:53], v227 offset:53248
	ds_read_b128 v[54:57], v227 offset:54272
	ds_read_b128 v[58:61], v227 offset:55296
	ds_read_b128 v[62:65], v227 offset:56320
	global_load_lds_dwordx4 v[222:223], off
	s_add_i32 m0, s48, 0x2000
	s_add_u32 s46, s46, 0x40080
	v_lshl_add_u64 v[220:221], v[220:221], 0, s[12:13]
	s_addc_u32 s47, s47, 0
	s_add_i32 s48, s51, s56
	global_load_lds_dwordx4 v[220:221], off
	v_lshl_add_u64 v[220:221], s[46:47], 0, v[200:201]
	s_mov_b32 m0, s48
	v_lshl_add_u64 v[216:217], v[216:217], 0, s[12:13]
	global_load_lds_dwordx4 v[220:221], off
	v_lshl_add_u64 v[220:221], s[46:47], 0, v[194:195]
	s_add_i32 m0, s48, 0x2000
	s_nop 0
	global_load_lds_dwordx4 v[220:221], off
	s_mov_b32 m0, s65
	s_nop 0
	global_load_lds_dwordx4 v[216:217], off
	v_lshl_add_u64 v[216:217], v[218:219], 0, s[12:13]
	s_mov_b32 m0, s66
	s_nop 0
	global_load_lds_dwordx4 v[216:217], off
	s_waitcnt vmcnt(8)
	s_waitcnt lgkmcnt(0)
	s_barrier
	s_setprio 1
	s_waitcnt lgkmcnt(0)
	v_mfma_scale_f32_16x16x128_f8f6f4 v[126:129], v[2:9], v[34:41], v[126:129], v228, v228 op_sel_hi:[0,0,0]
	v_mfma_scale_f32_16x16x128_f8f6f4 v[122:125], v[10:17], v[34:41], v[122:125], v228, v228 op_sel_hi:[0,0,0]
	v_mfma_scale_f32_16x16x128_f8f6f4 v[114:117], v[2:9], v[42:49], v[114:117], v228, v228 op_sel_hi:[0,0,0]
	v_mfma_scale_f32_16x16x128_f8f6f4 v[106:109], v[10:17], v[42:49], v[106:109], v228, v228 op_sel_hi:[0,0,0]
	v_mfma_scale_f32_16x16x128_f8f6f4 v[98:101], v[2:9], v[50:57], v[98:101], v228, v228 op_sel_hi:[0,0,0]
	v_mfma_scale_f32_16x16x128_f8f6f4 v[90:93], v[10:17], v[50:57], v[90:93], v228, v228 op_sel_hi:[0,0,0]
	v_mfma_scale_f32_16x16x128_f8f6f4 v[82:85], v[2:9], v[58:65], v[82:85], v228, v228 op_sel_hi:[0,0,0]
	v_mfma_scale_f32_16x16x128_f8f6f4 v[74:77], v[10:17], v[58:65], v[74:77], v228, v228 op_sel_hi:[0,0,0]
	s_setprio 0
	s_setprio 1
	v_mfma_scale_f32_16x16x128_f8f6f4 v[118:121], v[18:25], v[34:41], v[118:121], v228, v228 op_sel_hi:[0,0,0]
	v_mfma_scale_f32_16x16x128_f8f6f4 v[110:113], v[26:33], v[34:41], v[110:113], v228, v228 op_sel_hi:[0,0,0]
	v_mfma_scale_f32_16x16x128_f8f6f4 v[102:105], v[18:25], v[42:49], v[102:105], v228, v228 op_sel_hi:[0,0,0]
	v_mfma_scale_f32_16x16x128_f8f6f4 v[94:97], v[26:33], v[42:49], v[94:97], v228, v228 op_sel_hi:[0,0,0]
	v_mfma_scale_f32_16x16x128_f8f6f4 v[86:89], v[18:25], v[50:57], v[86:89], v228, v228 op_sel_hi:[0,0,0]
	v_mfma_scale_f32_16x16x128_f8f6f4 v[78:81], v[26:33], v[50:57], v[78:81], v228, v228 op_sel_hi:[0,0,0]
	v_mfma_scale_f32_16x16x128_f8f6f4 v[70:73], v[18:25], v[58:65], v[70:73], v228, v228 op_sel_hi:[0,0,0]
	v_mfma_scale_f32_16x16x128_f8f6f4 v[66:69], v[26:33], v[58:65], v[66:69], v228, v228 op_sel_hi:[0,0,0]
	s_setprio 0
	s_barrier
	s_add_i32 s77, s77, 2
	s_add_u32 s42, s42, 0x100
	s_addc_u32 s43, s43, 0
	s_cmp_gt_u32 s77, 13
	s_cbranch_scc1 .LBB0_1363

.LBB0_1365:
	s_ashr_i32 s40, s38, 3
	s_lshl_b32 s27, s38, 8
	s_ashr_i32 s41, s40, 31
	s_and_b32 s27, s27, 0x700
	s_lshl_b64 s[40:41], s[40:41], 13
	v_or_b32_e32 v204, s27, v224
	s_add_u32 s40, s2, s40
	s_addc_u32 s41, s3, s41
	v_lshlrev_b32_e32 v2, 2, v204
	v_mov_b32_e32 v3, v205
	s_nop 15
	s_nop 15
	v_lshl_add_u64 v[2:3], s[40:41], 0, v[2:3]
	flat_load_dwordx4 v[14:17], v[2:3]
	flat_load_dwordx4 v[10:13], v[2:3] offset:16
	flat_load_dwordx4 v[6:9], v[2:3] offset:128
	s_nop 0
	flat_load_dwordx4 v[2:5], v[2:3] offset:144
	v_lshl_add_u32 v20, s36, 8, v1
	v_mbcnt_lo_u32_b32 v22, -1, 0
	v_ashrrev_i32_e32 v21, 31, v20
	v_mbcnt_hi_u32_b32 v22, -1, v22
	v_lshlrev_b64 v[20:21], 11, v[20:21]
	v_and_b32_e32 v22, 16, v22
	v_lshl_add_u64 v[20:21], s[10:11], 0, v[20:21]
	v_lshrrev_b32_e32 v23, 1, v22
	v_add_u32_e32 v22, v22, v23
	v_lshl_add_u64 v[18:19], v[20:21], 0, v[204:205]
	v_mov_b32_e32 v23, v205
	v_mov_b32_e32 v24, 0x8000
	v_mov_b32_e32 v25, v205
	v_mov_b32_e32 v26, 0x28000
	v_mov_b32_e32 v27, v205
	v_lshl_add_u64 v[18:19], v[18:19], 0, v[22:23]
	s_waitcnt vmcnt(0) lgkmcnt(0)
	v_pk_fma_f32 v[28:29], v[190:191], s[16:17], v[14:15] op_sel_hi:[1,0,1]
	v_pk_fma_f32 v[30:31], v[192:193], s[16:17], v[16:17] op_sel_hi:[1,0,1]
	v_pk_fma_f32 v[32:33], v[186:187], s[16:17], v[10:11] op_sel_hi:[1,0,1]
	v_pk_fma_f32 v[34:35], v[188:189], s[16:17], v[12:13] op_sel_hi:[1,0,1]
	v_pk_fma_f32 v[36:37], v[170:171], s[16:17], v[6:7] op_sel_hi:[1,0,1]
	v_pk_fma_f32 v[38:39], v[172:173], s[16:17], v[8:9] op_sel_hi:[1,0,1]
	v_pk_fma_f32 v[40:41], v[166:167], s[16:17], v[2:3] op_sel_hi:[1,0,1]
	v_pk_fma_f32 v[42:43], v[168:169], s[16:17], v[4:5] op_sel_hi:[1,0,1]
	v_pk_mul_f32 v[28:29], v[28:29], s[18:19] op_sel_hi:[1,0]
	v_pk_mul_f32 v[30:31], v[30:31], s[18:19] op_sel_hi:[1,0]
	v_pk_mul_f32 v[32:33], v[32:33], s[18:19] op_sel_hi:[1,0]
	v_pk_mul_f32 v[34:35], v[34:35], s[18:19] op_sel_hi:[1,0]
	v_pk_mul_f32 v[36:37], v[36:37], s[18:19] op_sel_hi:[1,0]
	v_pk_mul_f32 v[38:39], v[38:39], s[18:19] op_sel_hi:[1,0]
	v_pk_mul_f32 v[40:41], v[40:41], s[18:19] op_sel_hi:[1,0]
	v_pk_mul_f32 v[42:43], v[42:43], s[18:19] op_sel_hi:[1,0]
	v_mov_b32_e32 v44, v205
	v_mov_b32_e32 v45, v205
	v_mov_b32_e32 v46, v205
	v_mov_b32_e32 v47, v205
	v_cvt_pk_fp8_f32 v44, v28, v29
	v_cvt_pk_fp8_f32 v45, v32, v33
	v_cvt_pk_fp8_f32 v46, v36, v37
	v_cvt_pk_fp8_f32 v47, v40, v41
	v_cvt_pk_fp8_f32 v44, v30, v31 op_sel:[0,0,1]
	v_cvt_pk_fp8_f32 v45, v34, v35 op_sel:[0,0,1]
	v_cvt_pk_fp8_f32 v46, v38, v39 op_sel:[0,0,1]
	v_cvt_pk_fp8_f32 v47, v42, v43 op_sel:[0,0,1]
	s_nop 1
	v_permlane16_swap_b32 v44, v46
	v_permlane16_swap_b32 v45, v47
	s_nop 1
	global_store_dwordx4 v[18:19], v[44:47], off
	v_lshl_add_u64 v[18:19], v[18:19], 0, v[24:25]
	v_pk_fma_f32 v[28:29], v[182:183], s[16:17], v[14:15] op_sel_hi:[1,0,1]
	v_pk_fma_f32 v[30:31], v[184:185], s[16:17], v[16:17] op_sel_hi:[1,0,1]
	v_pk_fma_f32 v[32:33], v[178:179], s[16:17], v[10:11] op_sel_hi:[1,0,1]
	v_pk_fma_f32 v[34:35], v[180:181], s[16:17], v[12:13] op_sel_hi:[1,0,1]
	v_pk_fma_f32 v[36:37], v[162:163], s[16:17], v[6:7] op_sel_hi:[1,0,1]
	v_pk_fma_f32 v[38:39], v[164:165], s[16:17], v[8:9] op_sel_hi:[1,0,1]
	v_pk_fma_f32 v[40:41], v[158:159], s[16:17], v[2:3] op_sel_hi:[1,0,1]
	v_pk_fma_f32 v[42:43], v[160:161], s[16:17], v[4:5] op_sel_hi:[1,0,1]
	v_pk_mul_f32 v[28:29], v[28:29], s[18:19] op_sel_hi:[1,0]
	v_pk_mul_f32 v[30:31], v[30:31], s[18:19] op_sel_hi:[1,0]
	v_pk_mul_f32 v[32:33], v[32:33], s[18:19] op_sel_hi:[1,0]
	v_pk_mul_f32 v[34:35], v[34:35], s[18:19] op_sel_hi:[1,0]
	v_pk_mul_f32 v[36:37], v[36:37], s[18:19] op_sel_hi:[1,0]
	v_pk_mul_f32 v[38:39], v[38:39], s[18:19] op_sel_hi:[1,0]
	v_pk_mul_f32 v[40:41], v[40:41], s[18:19] op_sel_hi:[1,0]
	v_pk_mul_f32 v[42:43], v[42:43], s[18:19] op_sel_hi:[1,0]
	v_mov_b32_e32 v48, v205
	v_mov_b32_e32 v49, v205
	v_mov_b32_e32 v50, v205
	v_mov_b32_e32 v51, v205
	v_cvt_pk_fp8_f32 v48, v28, v29
	v_cvt_pk_fp8_f32 v49, v32, v33
	v_cvt_pk_fp8_f32 v50, v36, v37
	v_cvt_pk_fp8_f32 v51, v40, v41
	v_cvt_pk_fp8_f32 v48, v30, v31 op_sel:[0,0,1]
	v_cvt_pk_fp8_f32 v49, v34, v35 op_sel:[0,0,1]
	v_cvt_pk_fp8_f32 v50, v38, v39 op_sel:[0,0,1]
	v_cvt_pk_fp8_f32 v51, v42, v43 op_sel:[0,0,1]
	s_nop 1
	v_permlane16_swap_b32 v48, v50
	v_permlane16_swap_b32 v49, v51
	s_nop 1
	global_store_dwordx4 v[18:19], v[48:51], off
	v_lshl_add_u64 v[18:19], v[18:19], 0, v[24:25]
	v_pk_fma_f32 v[28:29], v[174:175], s[16:17], v[14:15] op_sel_hi:[1,0,1]
	v_pk_fma_f32 v[30:31], v[176:177], s[16:17], v[16:17] op_sel_hi:[1,0,1]
	v_pk_fma_f32 v[32:33], v[154:155], s[16:17], v[10:11] op_sel_hi:[1,0,1]
	v_pk_fma_f32 v[34:35], v[156:157], s[16:17], v[12:13] op_sel_hi:[1,0,1]
	v_pk_fma_f32 v[36:37], v[150:151], s[16:17], v[6:7] op_sel_hi:[1,0,1]
	v_pk_fma_f32 v[38:39], v[152:153], s[16:17], v[8:9] op_sel_hi:[1,0,1]
	v_pk_fma_f32 v[40:41], v[142:143], s[16:17], v[2:3] op_sel_hi:[1,0,1]
	v_pk_fma_f32 v[42:43], v[144:145], s[16:17], v[4:5] op_sel_hi:[1,0,1]
	v_pk_mul_f32 v[28:29], v[28:29], s[18:19] op_sel_hi:[1,0]
	v_pk_mul_f32 v[30:31], v[30:31], s[18:19] op_sel_hi:[1,0]
	v_pk_mul_f32 v[32:33], v[32:33], s[18:19] op_sel_hi:[1,0]
	v_pk_mul_f32 v[34:35], v[34:35], s[18:19] op_sel_hi:[1,0]
	v_pk_mul_f32 v[36:37], v[36:37], s[18:19] op_sel_hi:[1,0]
	v_pk_mul_f32 v[38:39], v[38:39], s[18:19] op_sel_hi:[1,0]
	v_pk_mul_f32 v[40:41], v[40:41], s[18:19] op_sel_hi:[1,0]
	v_pk_mul_f32 v[42:43], v[42:43], s[18:19] op_sel_hi:[1,0]
	v_mov_b32_e32 v44, v205
	v_mov_b32_e32 v45, v205
	v_mov_b32_e32 v46, v205
	v_mov_b32_e32 v47, v205
	v_cvt_pk_fp8_f32 v44, v28, v29
	v_cvt_pk_fp8_f32 v45, v32, v33
	v_cvt_pk_fp8_f32 v46, v36, v37
	v_cvt_pk_fp8_f32 v47, v40, v41
	v_cvt_pk_fp8_f32 v44, v30, v31 op_sel:[0,0,1]
	v_cvt_pk_fp8_f32 v45, v34, v35 op_sel:[0,0,1]
	v_cvt_pk_fp8_f32 v46, v38, v39 op_sel:[0,0,1]
	v_cvt_pk_fp8_f32 v47, v42, v43 op_sel:[0,0,1]
	s_nop 1
	v_permlane16_swap_b32 v44, v46
	v_permlane16_swap_b32 v45, v47
	s_nop 1
	global_store_dwordx4 v[18:19], v[44:47], off
	v_lshl_add_u64 v[18:19], v[18:19], 0, v[24:25]
	v_pk_fma_f32 v[28:29], v[146:147], s[16:17], v[14:15] op_sel_hi:[1,0,1]
	v_pk_fma_f32 v[30:31], v[148:149], s[16:17], v[16:17] op_sel_hi:[1,0,1]
	v_pk_fma_f32 v[32:33], v[138:139], s[16:17], v[10:11] op_sel_hi:[1,0,1]
	v_pk_fma_f32 v[34:35], v[140:141], s[16:17], v[12:13] op_sel_hi:[1,0,1]
	v_pk_fma_f32 v[36:37], v[134:135], s[16:17], v[6:7] op_sel_hi:[1,0,1]
	v_pk_fma_f32 v[38:39], v[136:137], s[16:17], v[8:9] op_sel_hi:[1,0,1]
	v_pk_fma_f32 v[40:41], v[130:131], s[16:17], v[2:3] op_sel_hi:[1,0,1]
	v_pk_fma_f32 v[42:43], v[132:133], s[16:17], v[4:5] op_sel_hi:[1,0,1]
	v_pk_mul_f32 v[28:29], v[28:29], s[18:19] op_sel_hi:[1,0]
	v_pk_mul_f32 v[30:31], v[30:31], s[18:19] op_sel_hi:[1,0]
	v_pk_mul_f32 v[32:33], v[32:33], s[18:19] op_sel_hi:[1,0]
	v_pk_mul_f32 v[34:35], v[34:35], s[18:19] op_sel_hi:[1,0]
	v_pk_mul_f32 v[36:37], v[36:37], s[18:19] op_sel_hi:[1,0]
	v_pk_mul_f32 v[38:39], v[38:39], s[18:19] op_sel_hi:[1,0]
	v_pk_mul_f32 v[40:41], v[40:41], s[18:19] op_sel_hi:[1,0]
	v_pk_mul_f32 v[42:43], v[42:43], s[18:19] op_sel_hi:[1,0]
	v_mov_b32_e32 v48, v205
	v_mov_b32_e32 v49, v205
	v_mov_b32_e32 v50, v205
	v_mov_b32_e32 v51, v205
	v_cvt_pk_fp8_f32 v48, v28, v29
	v_cvt_pk_fp8_f32 v49, v32, v33
	v_cvt_pk_fp8_f32 v50, v36, v37
	v_cvt_pk_fp8_f32 v51, v40, v41
	v_cvt_pk_fp8_f32 v48, v30, v31 op_sel:[0,0,1]
	v_cvt_pk_fp8_f32 v49, v34, v35 op_sel:[0,0,1]
	v_cvt_pk_fp8_f32 v50, v38, v39 op_sel:[0,0,1]
	v_cvt_pk_fp8_f32 v51, v42, v43 op_sel:[0,0,1]
	s_nop 1
	v_permlane16_swap_b32 v48, v50
	v_permlane16_swap_b32 v49, v51
	s_nop 1
	global_store_dwordx4 v[18:19], v[48:51], off
	v_lshl_add_u64 v[18:19], v[18:19], 0, v[26:27]
	v_pk_fma_f32 v[28:29], v[126:127], s[16:17], v[14:15] op_sel_hi:[1,0,1]
	v_pk_fma_f32 v[30:31], v[128:129], s[16:17], v[16:17] op_sel_hi:[1,0,1]
	v_pk_fma_f32 v[32:33], v[122:123], s[16:17], v[10:11] op_sel_hi:[1,0,1]
	v_pk_fma_f32 v[34:35], v[124:125], s[16:17], v[12:13] op_sel_hi:[1,0,1]
	v_pk_fma_f32 v[36:37], v[118:119], s[16:17], v[6:7] op_sel_hi:[1,0,1]
	v_pk_fma_f32 v[38:39], v[120:121], s[16:17], v[8:9] op_sel_hi:[1,0,1]
	v_pk_fma_f32 v[40:41], v[110:111], s[16:17], v[2:3] op_sel_hi:[1,0,1]
	v_pk_fma_f32 v[42:43], v[112:113], s[16:17], v[4:5] op_sel_hi:[1,0,1]
	v_pk_mul_f32 v[28:29], v[28:29], s[18:19] op_sel_hi:[1,0]
	v_pk_mul_f32 v[30:31], v[30:31], s[18:19] op_sel_hi:[1,0]
	v_pk_mul_f32 v[32:33], v[32:33], s[18:19] op_sel_hi:[1,0]
	v_pk_mul_f32 v[34:35], v[34:35], s[18:19] op_sel_hi:[1,0]
	v_pk_mul_f32 v[36:37], v[36:37], s[18:19] op_sel_hi:[1,0]
	v_pk_mul_f32 v[38:39], v[38:39], s[18:19] op_sel_hi:[1,0]
	v_pk_mul_f32 v[40:41], v[40:41], s[18:19] op_sel_hi:[1,0]
	v_pk_mul_f32 v[42:43], v[42:43], s[18:19] op_sel_hi:[1,0]
	v_mov_b32_e32 v44, v205
	v_mov_b32_e32 v45, v205
	v_mov_b32_e32 v46, v205
	v_mov_b32_e32 v47, v205
	v_cvt_pk_fp8_f32 v44, v28, v29
	v_cvt_pk_fp8_f32 v45, v32, v33
	v_cvt_pk_fp8_f32 v46, v36, v37
	v_cvt_pk_fp8_f32 v47, v40, v41
	v_cvt_pk_fp8_f32 v44, v30, v31 op_sel:[0,0,1]
	v_cvt_pk_fp8_f32 v45, v34, v35 op_sel:[0,0,1]
	v_cvt_pk_fp8_f32 v46, v38, v39 op_sel:[0,0,1]
	v_cvt_pk_fp8_f32 v47, v42, v43 op_sel:[0,0,1]
	s_nop 1
	v_permlane16_swap_b32 v44, v46
	v_permlane16_swap_b32 v45, v47
	s_nop 1
	global_store_dwordx4 v[18:19], v[44:47], off
	v_lshl_add_u64 v[18:19], v[18:19], 0, v[24:25]
	v_pk_fma_f32 v[28:29], v[114:115], s[16:17], v[14:15] op_sel_hi:[1,0,1]
	v_pk_fma_f32 v[30:31], v[116:117], s[16:17], v[16:17] op_sel_hi:[1,0,1]
	v_pk_fma_f32 v[32:33], v[106:107], s[16:17], v[10:11] op_sel_hi:[1,0,1]
	v_pk_fma_f32 v[34:35], v[108:109], s[16:17], v[12:13] op_sel_hi:[1,0,1]
	v_pk_fma_f32 v[36:37], v[102:103], s[16:17], v[6:7] op_sel_hi:[1,0,1]
	v_pk_fma_f32 v[38:39], v[104:105], s[16:17], v[8:9] op_sel_hi:[1,0,1]
	v_pk_fma_f32 v[40:41], v[94:95], s[16:17], v[2:3] op_sel_hi:[1,0,1]
	v_pk_fma_f32 v[42:43], v[96:97], s[16:17], v[4:5] op_sel_hi:[1,0,1]
	v_pk_mul_f32 v[28:29], v[28:29], s[18:19] op_sel_hi:[1,0]
	v_pk_mul_f32 v[30:31], v[30:31], s[18:19] op_sel_hi:[1,0]
	v_pk_mul_f32 v[32:33], v[32:33], s[18:19] op_sel_hi:[1,0]
	v_pk_mul_f32 v[34:35], v[34:35], s[18:19] op_sel_hi:[1,0]
	v_pk_mul_f32 v[36:37], v[36:37], s[18:19] op_sel_hi:[1,0]
	v_pk_mul_f32 v[38:39], v[38:39], s[18:19] op_sel_hi:[1,0]
	v_pk_mul_f32 v[40:41], v[40:41], s[18:19] op_sel_hi:[1,0]
	v_pk_mul_f32 v[42:43], v[42:43], s[18:19] op_sel_hi:[1,0]
	v_mov_b32_e32 v48, v205
	v_mov_b32_e32 v49, v205
	v_mov_b32_e32 v50, v205
	v_mov_b32_e32 v51, v205
	v_cvt_pk_fp8_f32 v48, v28, v29
	v_cvt_pk_fp8_f32 v49, v32, v33
	v_cvt_pk_fp8_f32 v50, v36, v37
	v_cvt_pk_fp8_f32 v51, v40, v41
	v_cvt_pk_fp8_f32 v48, v30, v31 op_sel:[0,0,1]
	v_cvt_pk_fp8_f32 v49, v34, v35 op_sel:[0,0,1]
	v_cvt_pk_fp8_f32 v50, v38, v39 op_sel:[0,0,1]
	v_cvt_pk_fp8_f32 v51, v42, v43 op_sel:[0,0,1]
	s_nop 1
	v_permlane16_swap_b32 v48, v50
	v_permlane16_swap_b32 v49, v51
	s_nop 1
	global_store_dwordx4 v[18:19], v[48:51], off
	v_lshl_add_u64 v[18:19], v[18:19], 0, v[24:25]
	v_pk_fma_f32 v[28:29], v[98:99], s[16:17], v[14:15] op_sel_hi:[1,0,1]
	v_pk_fma_f32 v[30:31], v[100:101], s[16:17], v[16:17] op_sel_hi:[1,0,1]
	v_pk_fma_f32 v[32:33], v[90:91], s[16:17], v[10:11] op_sel_hi:[1,0,1]
	v_pk_fma_f32 v[34:35], v[92:93], s[16:17], v[12:13] op_sel_hi:[1,0,1]
	v_pk_fma_f32 v[36:37], v[86:87], s[16:17], v[6:7] op_sel_hi:[1,0,1]
	v_pk_fma_f32 v[38:39], v[88:89], s[16:17], v[8:9] op_sel_hi:[1,0,1]
	v_pk_fma_f32 v[40:41], v[78:79], s[16:17], v[2:3] op_sel_hi:[1,0,1]
	v_pk_fma_f32 v[42:43], v[80:81], s[16:17], v[4:5] op_sel_hi:[1,0,1]
	v_pk_mul_f32 v[28:29], v[28:29], s[18:19] op_sel_hi:[1,0]
	v_pk_mul_f32 v[30:31], v[30:31], s[18:19] op_sel_hi:[1,0]
	v_pk_mul_f32 v[32:33], v[32:33], s[18:19] op_sel_hi:[1,0]
	v_pk_mul_f32 v[34:35], v[34:35], s[18:19] op_sel_hi:[1,0]
	v_pk_mul_f32 v[36:37], v[36:37], s[18:19] op_sel_hi:[1,0]
	v_pk_mul_f32 v[38:39], v[38:39], s[18:19] op_sel_hi:[1,0]
	v_pk_mul_f32 v[40:41], v[40:41], s[18:19] op_sel_hi:[1,0]
	v_pk_mul_f32 v[42:43], v[42:43], s[18:19] op_sel_hi:[1,0]
	v_mov_b32_e32 v44, v205
	v_mov_b32_e32 v45, v205
	v_mov_b32_e32 v46, v205
	v_mov_b32_e32 v47, v205
	v_cvt_pk_fp8_f32 v44, v28, v29
	v_cvt_pk_fp8_f32 v45, v32, v33
	v_cvt_pk_fp8_f32 v46, v36, v37
	v_cvt_pk_fp8_f32 v47, v40, v41
	v_cvt_pk_fp8_f32 v44, v30, v31 op_sel:[0,0,1]
	v_cvt_pk_fp8_f32 v45, v34, v35 op_sel:[0,0,1]
	v_cvt_pk_fp8_f32 v46, v38, v39 op_sel:[0,0,1]
	v_cvt_pk_fp8_f32 v47, v42, v43 op_sel:[0,0,1]
	s_nop 1
	v_permlane16_swap_b32 v44, v46
	v_permlane16_swap_b32 v45, v47
	s_nop 1
	global_store_dwordx4 v[18:19], v[44:47], off
	v_lshl_add_u64 v[18:19], v[18:19], 0, v[24:25]
	v_pk_fma_f32 v[28:29], v[82:83], s[16:17], v[14:15] op_sel_hi:[1,0,1]
	v_pk_fma_f32 v[30:31], v[84:85], s[16:17], v[16:17] op_sel_hi:[1,0,1]
	v_pk_fma_f32 v[32:33], v[74:75], s[16:17], v[10:11] op_sel_hi:[1,0,1]
	v_pk_fma_f32 v[34:35], v[76:77], s[16:17], v[12:13] op_sel_hi:[1,0,1]
	v_pk_fma_f32 v[36:37], v[70:71], s[16:17], v[6:7] op_sel_hi:[1,0,1]
	v_pk_fma_f32 v[38:39], v[72:73], s[16:17], v[8:9] op_sel_hi:[1,0,1]
	v_pk_fma_f32 v[40:41], v[66:67], s[16:17], v[2:3] op_sel_hi:[1,0,1]
	v_pk_fma_f32 v[42:43], v[68:69], s[16:17], v[4:5] op_sel_hi:[1,0,1]
	v_pk_mul_f32 v[28:29], v[28:29], s[18:19] op_sel_hi:[1,0]
	v_pk_mul_f32 v[30:31], v[30:31], s[18:19] op_sel_hi:[1,0]
	v_pk_mul_f32 v[32:33], v[32:33], s[18:19] op_sel_hi:[1,0]
	v_pk_mul_f32 v[34:35], v[34:35], s[18:19] op_sel_hi:[1,0]
	v_pk_mul_f32 v[36:37], v[36:37], s[18:19] op_sel_hi:[1,0]
	v_pk_mul_f32 v[38:39], v[38:39], s[18:19] op_sel_hi:[1,0]
	v_pk_mul_f32 v[40:41], v[40:41], s[18:19] op_sel_hi:[1,0]
	v_pk_mul_f32 v[42:43], v[42:43], s[18:19] op_sel_hi:[1,0]
	v_mov_b32_e32 v48, v205
	v_mov_b32_e32 v49, v205
	v_mov_b32_e32 v50, v205
	v_mov_b32_e32 v51, v205
	v_cvt_pk_fp8_f32 v48, v28, v29
	v_cvt_pk_fp8_f32 v49, v32, v33
	v_cvt_pk_fp8_f32 v50, v36, v37
	v_cvt_pk_fp8_f32 v51, v40, v41
	v_cvt_pk_fp8_f32 v48, v30, v31 op_sel:[0,0,1]
	v_cvt_pk_fp8_f32 v49, v34, v35 op_sel:[0,0,1]
	v_cvt_pk_fp8_f32 v50, v38, v39 op_sel:[0,0,1]
	v_cvt_pk_fp8_f32 v51, v42, v43 op_sel:[0,0,1]
	s_nop 1
	v_permlane16_swap_b32 v48, v50
	v_permlane16_swap_b32 v49, v51
	s_nop 1
	global_store_dwordx4 v[18:19], v[48:51], off
	s_andn2_b64 vcc, exec, s[8:9]
	s_mov_b64 s[8:9], -1
	s_cbranch_vccnz .LBB0_1350
	s_andn2_b64 vcc, exec, s[6:7]
	s_cbranch_vccnz .LBB0_1349
	s_barrier
	s_branch .LBB0_1349
